# combo8 + k-rope cos/sin rows also loaded at the top of the prep unit (31 loads in flight per unit)
# baseline (speedup 1.0000x reference)
.LBB0_310:
	s_and_b32 s27, s25, 0x7c0
	v_add_u32_e32 v88, s27, v96
	v_add_u32_e32 v34, s25, v96
	v_mov_b64_e32 v[32:33], s[10:11]
	v_mad_i64_i32 v[90:91], s[6:7], v34, s71, v[32:33]
	v_lshlrev_b32_e32 v32, 5, v88
	v_ashrrev_i32_e32 v33, 31, v32
	v_lshlrev_b64 v[36:37], 2, v[32:33]
	v_lshl_add_u64 v[32:33], v[66:67], 0, v[36:37]
	v_lshl_add_u64 v[36:37], v[68:69], 0, v[36:37]
	s_barrier
	global_load_dwordx4 v[32:35], v[32:33], off
	v_lshl_add_u64 v[40:41], v[90:91], 0, v[184:185]
	global_load_dwordx4 v[36:39], v[36:37], off
	v_add_co_u32_e32 v40, vcc, s86, v40
	v_mov_b32_e32 v81, v185
	s_nop 0
	v_addc_co_u32_e32 v41, vcc, 0, v41, vcc
	global_load_dwordx2 v[42:43], v[40:41], off offset:512
	global_load_dwordx2 v[44:45], v[40:41], off offset:576
	global_load_dwordx2 v[46:47], v[40:41], off offset:640
	global_load_dwordx2 v[48:49], v[40:41], off offset:704
	global_load_dwordx2 v[50:51], v[40:41], off offset:768
	global_load_dwordx2 v[52:53], v[40:41], off offset:832
	global_load_dwordx2 v[54:55], v[40:41], off offset:896
	global_load_dwordx2 v[56:57], v[40:41], off offset:960
	v_mov_b32_e32 v83, v185
	s_mov_b64 s[6:7], 0x1500
	v_lshlrev_b32_e32 v114, 4, v88
	v_ashrrev_i32_e32 v115, 31, v114
	v_lshlrev_b64 v[114:115], 2, v[114:115]
	v_lshl_add_u64 v[116:117], v[70:71], 0, v[114:115]
	v_lshl_add_u64 v[118:119], v[72:73], 0, v[114:115]
	v_lshl_add_u64 v[114:115], v[90:91], 0, v[80:81]
	global_load_dwordx4 v[124:127], v[116:117], off offset:16
	global_load_dwordx4 v[128:131], v[116:117], off
	v_lshl_add_u64 v[114:115], v[114:115], 0, v[82:83]
	global_load_dwordx4 v[132:135], v[118:119], off offset:16
	global_load_dwordx4 v[136:139], v[118:119], off
	v_lshl_add_u64 v[116:117], v[114:115], 0, s[6:7]
	v_lshl_add_u64 v[118:119], v[90:91], 0, v[82:83]
	s_mov_b64 s[20:21], 0x1600
	global_load_dwordx4 v[140:143], v[116:117], off
	global_load_dwordx4 v[144:147], v[116:117], off offset:32
	v_lshl_add_u64 v[118:119], v[118:119], 0, s[20:21]
	s_mov_b64 s[30:31], 0x1000
	s_add_i32 s20, s24, s25
	global_load_dwordx4 v[148:151], v[118:119], off
	global_load_dwordx4 v[152:155], v[118:119], off offset:32
	v_lshl_add_u64 v[116:117], v[90:91], 0, s[30:31]
	s_mul_i32 s21, s20, 0x1800
	s_mul_hi_i32 s23, s20, 0x1800
	s_add_u32 s22, s10, s21
	s_addc_u32 s23, s11, s23
	v_mov_b32_e32 v85, v185
	global_load_dwordx2 v[156:157], v[116:117], off offset:1608
	v_lshl_add_u64 v[118:119], s[22:23], 0, v[84:85]
	s_mov_b64 s[20:21], 0x1800
	v_lshl_add_u64 v[118:119], v[118:119], 0, s[30:31]
	global_load_dword v158, v[118:119], off offset:1024
	v_lshl_add_u64 v[118:119], v[118:119], 0, s[20:21]
	global_load_dword v159, v[118:119], off offset:1024
	v_lshl_add_u64 v[118:119], v[118:119], 0, s[20:21]
	global_load_dword v160, v[118:119], off offset:1024
	v_lshl_add_u64 v[118:119], v[118:119], 0, s[20:21]
	global_load_dword v161, v[118:119], off offset:1024
	v_lshl_add_u64 v[118:119], v[118:119], 0, s[20:21]
	global_load_dword v162, v[118:119], off offset:1024
	v_lshl_add_u64 v[118:119], v[118:119], 0, s[20:21]
	global_load_dword v163, v[118:119], off offset:1024
	v_lshl_add_u64 v[118:119], v[118:119], 0, s[20:21]
	global_load_dword v164, v[118:119], off offset:1024
	v_lshl_add_u64 v[118:119], v[118:119], 0, s[20:21]
	global_load_dword v165, v[118:119], off offset:1024
	v_or_b32_e32 v114, s27, v97
	v_or_b32_e32 v116, s27, v99
	v_lshlrev_b32_e32 v114, 7, v114
	v_mov_b32_e32 v115, v185
	v_lshlrev_b32_e32 v116, 7, v116
	v_mov_b32_e32 v117, v185
	v_lshl_add_u64 v[118:119], v[74:75], 0, v[114:115]
	global_load_dwordx4 v[166:169], v[118:119], off
	v_lshl_add_u64 v[118:119], v[76:77], 0, v[114:115]
	global_load_dwordx4 v[170:173], v[118:119], off
	v_lshl_add_u64 v[118:119], v[74:75], 0, v[116:117]
	global_load_dwordx4 v[174:177], v[118:119], off
	v_lshl_add_u64 v[118:119], v[76:77], 0, v[116:117]
	global_load_dwordx4 v[178:181], v[118:119], off
	s_waitcnt vmcnt(28)
	v_lshlrev_b32_e32 v58, 16, v42
	s_waitcnt vmcnt(27)
	v_lshlrev_b32_e32 v60, 16, v44
	v_and_b32_e32 v61, 0xffff0000, v44
	v_and_b32_e32 v59, 0xffff0000, v42
	v_pk_mul_f32 v[62:63], v[36:37], v[60:61]
	v_pk_mul_f32 v[60:61], v[32:33], v[60:61]
	v_pk_fma_f32 v[62:63], v[32:33], v[58:59], v[62:63] neg_lo:[0,0,1] neg_hi:[0,0,1]
	v_pk_fma_f32 v[58:59], v[36:37], v[58:59], v[60:61]
	v_lshlrev_b32_e32 v60, 16, v45
	v_and_b32_e32 v61, 0xffff0000, v45
	v_cvt_pk_bf16_f32 v42, v62, v63
	v_cvt_pk_bf16_f32 v44, v58, v59
	v_lshlrev_b32_e32 v58, 16, v43
	v_and_b32_e32 v59, 0xffff0000, v43
	v_pk_mul_f32 v[62:63], v[38:39], v[60:61]
	v_pk_mul_f32 v[60:61], v[34:35], v[60:61]
	v_pk_fma_f32 v[62:63], v[34:35], v[58:59], v[62:63] neg_lo:[0,0,1] neg_hi:[0,0,1]
	v_pk_fma_f32 v[58:59], v[38:39], v[58:59], v[60:61]
	v_cvt_pk_bf16_f32 v43, v62, v63
	v_cvt_pk_bf16_f32 v45, v58, v59
	global_store_dwordx2 v[40:41], v[42:43], off offset:512
	global_store_dwordx2 v[40:41], v[44:45], off offset:576
	s_waitcnt vmcnt(27)
	v_lshlrev_b32_e32 v44, 16, v48
	v_and_b32_e32 v45, 0xffff0000, v48
	v_lshlrev_b32_e32 v42, 16, v46
	v_and_b32_e32 v43, 0xffff0000, v46
	v_pk_mul_f32 v[58:59], v[36:37], v[44:45]
	v_pk_mul_f32 v[44:45], v[32:33], v[44:45]
	v_pk_fma_f32 v[58:59], v[32:33], v[42:43], v[58:59] neg_lo:[0,0,1] neg_hi:[0,0,1]
	v_lshlrev_b32_e32 v48, 16, v49
	v_and_b32_e32 v49, 0xffff0000, v49
	v_cvt_pk_bf16_f32 v46, v58, v59
	v_pk_fma_f32 v[42:43], v[36:37], v[42:43], v[44:45]
	v_lshlrev_b32_e32 v44, 16, v47
	v_and_b32_e32 v45, 0xffff0000, v47
	v_pk_mul_f32 v[58:59], v[38:39], v[48:49]
	v_pk_mul_f32 v[48:49], v[34:35], v[48:49]
	v_pk_fma_f32 v[58:59], v[34:35], v[44:45], v[58:59] neg_lo:[0,0,1] neg_hi:[0,0,1]
	v_pk_fma_f32 v[44:45], v[38:39], v[44:45], v[48:49]
	v_cvt_pk_bf16_f32 v42, v42, v43
	v_cvt_pk_bf16_f32 v47, v58, v59
	v_cvt_pk_bf16_f32 v43, v44, v45
	s_waitcnt vmcnt(25)
	v_lshlrev_b32_e32 v44, 16, v52
	v_and_b32_e32 v45, 0xffff0000, v52
	global_store_dwordx2 v[40:41], v[46:47], off offset:640
	global_store_dwordx2 v[40:41], v[42:43], off offset:704
	v_lshlrev_b32_e32 v42, 16, v50
	v_and_b32_e32 v43, 0xffff0000, v50
	v_pk_mul_f32 v[46:47], v[36:37], v[44:45]
	v_pk_mul_f32 v[44:45], v[32:33], v[44:45]
	v_lshlrev_b32_e32 v48, 16, v53
	v_and_b32_e32 v49, 0xffff0000, v53
	v_pk_fma_f32 v[46:47], v[32:33], v[42:43], v[46:47] neg_lo:[0,0,1] neg_hi:[0,0,1]
	v_pk_fma_f32 v[42:43], v[36:37], v[42:43], v[44:45]
	v_lshlrev_b32_e32 v44, 16, v51
	v_and_b32_e32 v45, 0xffff0000, v51
	v_pk_mul_f32 v[50:51], v[38:39], v[48:49]
	v_pk_mul_f32 v[48:49], v[34:35], v[48:49]
	v_pk_fma_f32 v[50:51], v[34:35], v[44:45], v[50:51] neg_lo:[0,0,1] neg_hi:[0,0,1]
	v_pk_fma_f32 v[44:45], v[38:39], v[44:45], v[48:49]
	v_cvt_pk_bf16_f32 v46, v46, v47
	v_cvt_pk_bf16_f32 v42, v42, v43
	v_cvt_pk_bf16_f32 v47, v50, v51
	v_cvt_pk_bf16_f32 v43, v44, v45
	s_waitcnt vmcnt(25)
	v_lshlrev_b32_e32 v44, 16, v56
	v_and_b32_e32 v45, 0xffff0000, v56
	global_store_dwordx2 v[40:41], v[46:47], off offset:768
	global_store_dwordx2 v[40:41], v[42:43], off offset:832
	v_lshlrev_b32_e32 v42, 16, v54
	v_and_b32_e32 v43, 0xffff0000, v54
	v_pk_mul_f32 v[46:47], v[36:37], v[44:45]
	v_lshl_add_u64 v[48:49], v[90:91], 0, v[80:81]
	v_pk_fma_f32 v[46:47], v[32:33], v[42:43], v[46:47] neg_lo:[0,0,1] neg_hi:[0,0,1]
	v_pk_mul_f32 v[32:33], v[32:33], v[44:45]
	v_cvt_pk_bf16_f32 v46, v46, v47
	v_pk_fma_f32 v[32:33], v[36:37], v[42:43], v[32:33]
	v_lshlrev_b32_e32 v42, 16, v57
	v_and_b32_e32 v43, 0xffff0000, v57
	v_lshlrev_b32_e32 v36, 16, v55
	v_and_b32_e32 v37, 0xffff0000, v55
	v_pk_mul_f32 v[44:45], v[38:39], v[42:43]
	v_cvt_pk_bf16_f32 v32, v32, v33
	v_pk_fma_f32 v[44:45], v[34:35], v[36:37], v[44:45] neg_lo:[0,0,1] neg_hi:[0,0,1]
	v_pk_mul_f32 v[34:35], v[34:35], v[42:43]
	v_cvt_pk_bf16_f32 v47, v44, v45
	v_pk_fma_f32 v[34:35], v[38:39], v[36:37], v[34:35]
	v_lshl_add_u64 v[48:49], v[48:49], 0, v[82:83]
	v_cvt_pk_bf16_f32 v33, v34, v35
	global_store_dwordx2 v[40:41], v[46:47], off offset:896
	global_store_dwordx2 v[40:41], v[32:33], off offset:960
	v_lshl_add_u64 v[94:95], v[48:49], 0, s[6:7]
	v_lshl_add_u64 v[50:51], v[90:91], 0, v[82:83]
	s_mov_b64 s[6:7], 0x1600
	s_nop 0
	v_lshl_add_u64 v[92:93], v[50:51], 0, s[6:7]
	s_waitcnt vmcnt(23)
	v_mov_b64_e32 v[32:33], v[124:125]
	v_mov_b64_e32 v[34:35], v[126:127]
	v_mov_b64_e32 v[40:41], v[128:129]
	v_mov_b64_e32 v[42:43], v[130:131]
	v_mov_b64_e32 v[36:37], v[132:133]
	v_mov_b64_e32 v[38:39], v[134:135]
	v_mov_b64_e32 v[44:45], v[136:137]
	v_mov_b64_e32 v[46:47], v[138:139]
	v_mov_b64_e32 v[48:49], v[140:141]
	v_mov_b64_e32 v[50:51], v[142:143]
	v_mov_b64_e32 v[52:53], v[144:145]
	v_mov_b64_e32 v[54:55], v[146:147]
	v_lshlrev_b32_e32 v106, 16, v52
	v_and_b32_e32 v107, 0xffff0000, v52
	v_lshlrev_b32_e32 v104, 16, v48
	v_and_b32_e32 v105, 0xffff0000, v48
	v_pk_mul_f32 v[108:109], v[44:45], v[106:107]
	v_pk_mul_f32 v[106:107], v[40:41], v[106:107]
	v_lshlrev_b32_e32 v52, 16, v53
	v_and_b32_e32 v53, 0xffff0000, v53
	v_pk_fma_f32 v[108:109], v[40:41], v[104:105], v[108:109] neg_lo:[0,0,1] neg_hi:[0,0,1]
	v_pk_fma_f32 v[104:105], v[44:45], v[104:105], v[106:107]
	v_lshlrev_b32_e32 v48, 16, v49
	v_and_b32_e32 v49, 0xffff0000, v49
	v_pk_mul_f32 v[106:107], v[46:47], v[52:53]
	v_pk_mul_f32 v[52:53], v[42:43], v[52:53]
	v_lshlrev_b32_e32 v110, 16, v54
	v_and_b32_e32 v111, 0xffff0000, v54
	v_pk_fma_f32 v[106:107], v[42:43], v[48:49], v[106:107] neg_lo:[0,0,1] neg_hi:[0,0,1]
	v_pk_fma_f32 v[52:53], v[46:47], v[48:49], v[52:53]
	v_lshlrev_b32_e32 v48, 16, v50
	v_and_b32_e32 v49, 0xffff0000, v50
	v_pk_mul_f32 v[112:113], v[36:37], v[110:111]
	v_pk_mul_f32 v[110:111], v[32:33], v[110:111]
	v_lshlrev_b32_e32 v54, 16, v55
	v_and_b32_e32 v55, 0xffff0000, v55
	v_pk_fma_f32 v[112:113], v[32:33], v[48:49], v[112:113] neg_lo:[0,0,1] neg_hi:[0,0,1]
	v_pk_fma_f32 v[110:111], v[36:37], v[48:49], v[110:111]
	v_cvt_pk_bf16_f32 v48, v104, v105
	v_cvt_pk_bf16_f32 v49, v52, v53
	v_lshlrev_b32_e32 v52, 16, v51
	v_and_b32_e32 v53, 0xffff0000, v51
	v_pk_mul_f32 v[104:105], v[38:39], v[54:55]
	v_pk_mul_f32 v[54:55], v[34:35], v[54:55]
	v_pk_fma_f32 v[104:105], v[34:35], v[52:53], v[104:105] neg_lo:[0,0,1] neg_hi:[0,0,1]
	v_pk_fma_f32 v[52:53], v[38:39], v[52:53], v[54:55]
	v_cvt_pk_bf16_f32 v54, v112, v113
	v_cvt_pk_bf16_f32 v51, v52, v53
	v_cvt_pk_bf16_f32 v52, v108, v109
	v_cvt_pk_bf16_f32 v53, v106, v107
	v_cvt_pk_bf16_f32 v55, v104, v105
	v_cvt_pk_bf16_f32 v50, v110, v111
	global_store_dwordx4 v[94:95], v[52:55], off
	global_store_dwordx4 v[94:95], v[48:51], off offset:32
	s_and_saveexec_b64 s[6:7], s[2:3]
	s_cbranch_execz .LBB0_314
	s_waitcnt vmcnt(23)
	v_mov_b64_e32 v[56:57], v[148:149]
	v_mov_b64_e32 v[58:59], v[150:151]
	v_mov_b64_e32 v[60:61], v[152:153]
	v_mov_b64_e32 v[62:63], v[154:155]
	v_lshlrev_b32_e32 v52, 16, v56
	v_and_b32_e32 v53, 0xffff0000, v56
	v_lshlrev_b32_e32 v50, 16, v60
	v_and_b32_e32 v51, 0xffff0000, v60
	v_pk_mul_f32 v[48:49], v[44:45], v[52:53]
	v_pk_mul_f32 v[44:45], v[44:45], v[50:51]
	v_pk_fma_f32 v[48:49], v[40:41], v[50:51], v[48:49]
	v_lshlrev_b32_e32 v50, 16, v57
	v_and_b32_e32 v51, 0xffff0000, v57
	v_pk_fma_f32 v[40:41], v[40:41], v[52:53], v[44:45] neg_lo:[0,0,1] neg_hi:[0,0,1]
	v_lshlrev_b32_e32 v44, 16, v61
	v_and_b32_e32 v45, 0xffff0000, v61
	v_pk_mul_f32 v[52:53], v[46:47], v[50:51]
	v_cvt_pk_bf16_f32 v40, v40, v41
	v_pk_fma_f32 v[52:53], v[42:43], v[44:45], v[52:53]
	v_pk_mul_f32 v[44:45], v[46:47], v[44:45]
	v_cvt_pk_bf16_f32 v48, v48, v49
	v_pk_fma_f32 v[42:43], v[42:43], v[50:51], v[44:45] neg_lo:[0,0,1] neg_hi:[0,0,1]
	v_lshlrev_b32_e32 v44, 16, v58
	v_cvt_pk_bf16_f32 v41, v42, v43
	v_lshlrev_b32_e32 v42, 16, v62
	v_and_b32_e32 v43, 0xffff0000, v62
	v_and_b32_e32 v45, 0xffff0000, v58
	v_pk_mul_f32 v[46:47], v[36:37], v[44:45]
	v_pk_mul_f32 v[36:37], v[36:37], v[42:43]
	v_pk_fma_f32 v[46:47], v[32:33], v[42:43], v[46:47]
	v_pk_fma_f32 v[32:33], v[32:33], v[44:45], v[36:37] neg_lo:[0,0,1] neg_hi:[0,0,1]
	v_lshlrev_b32_e32 v36, 16, v59
	v_and_b32_e32 v37, 0xffff0000, v59
	v_cvt_pk_bf16_f32 v42, v32, v33
	v_lshlrev_b32_e32 v32, 16, v63
	v_and_b32_e32 v33, 0xffff0000, v63
	v_pk_mul_f32 v[44:45], v[38:39], v[36:37]
	v_cvt_pk_bf16_f32 v49, v52, v53
	v_pk_fma_f32 v[44:45], v[34:35], v[32:33], v[44:45]
	v_pk_mul_f32 v[32:33], v[38:39], v[32:33]
	v_cvt_pk_bf16_f32 v50, v46, v47
	v_pk_fma_f32 v[32:33], v[34:35], v[36:37], v[32:33] neg_lo:[0,0,1] neg_hi:[0,0,1]
	v_cvt_pk_bf16_f32 v51, v44, v45
	v_cvt_pk_bf16_f32 v43, v32, v33
	global_store_dwordx4 v[92:93], v[40:43], off
	global_store_dwordx4 v[92:93], v[48:51], off offset:32
.LBB0_314:
	s_or_b64 exec, exec, s[6:7]
	s_ashr_i32 s28, s0, 5
	s_and_saveexec_b64 s[6:7], s[4:5]
	s_cbranch_execz .LBB0_316
	s_lshl_b32 s20, s28, 2
	s_mov_b32 s34, 0xbfb8aa3b
	v_ashrrev_i32_e32 v89, 31, v88
	s_ashr_i32 s21, s20, 31
	s_lshl_b64 s[30:31], s[20:21], 13
	s_waitcnt vmcnt(24)
	v_lshlrev_b32_e32 v34, 16, v156
	v_and_b32_e32 v36, 0xffff0000, v156
	v_add_f32_e32 v34, v120, v34
	v_min_f32_e32 v39, 0, v34
	v_mul_f32_e64 v34, |v34|, s34
	v_exp_f32_e32 v34, v34
	v_lshlrev_b32_e32 v37, 16, v157
	v_and_b32_e32 v38, 0xffff0000, v157
	v_lshl_add_u64 v[32:33], v[88:89], 2, s[16:17]
	v_add_f32_e32 v34, 1.0, v34
	v_log_f32_e32 v34, v34
	s_nop 0
	v_fmac_f32_e32 v39, 0xbf317218, v34
	v_lshl_add_u64 v[34:35], v[32:33], 0, s[30:31]
	global_store_dword v[34:35], v39, off
	s_or_b32 s30, s20, 1
	s_ashr_i32 s31, s30, 31
	s_lshl_b64 s[30:31], s[30:31], 13
	v_add_f32_e32 v34, v121, v36
	v_min_f32_e32 v36, 0, v34
	v_mul_f32_e64 v34, |v34|, s34
	v_exp_f32_e32 v34, v34
	s_nop 0
	v_add_f32_e32 v34, 1.0, v34
	v_log_f32_e32 v34, v34
	s_nop 0
	v_fmac_f32_e32 v36, 0xbf317218, v34
	v_lshl_add_u64 v[34:35], v[32:33], 0, s[30:31]
	global_store_dword v[34:35], v36, off
	s_or_b32 s30, s20, 2
	s_ashr_i32 s31, s30, 31
	s_lshl_b64 s[30:31], s[30:31], 13
	s_or_b32 s20, s20, 3
	s_ashr_i32 s21, s20, 31
	s_lshl_b64 s[20:21], s[20:21], 13
	v_add_f32_e32 v34, v122, v37
	v_min_f32_e32 v36, 0, v34
	v_mul_f32_e64 v34, |v34|, s34
	v_exp_f32_e32 v34, v34
	s_nop 0
	v_add_f32_e32 v34, 1.0, v34
	v_log_f32_e32 v34, v34
	s_nop 0
	v_fmac_f32_e32 v36, 0xbf317218, v34
	v_lshl_add_u64 v[34:35], v[32:33], 0, s[30:31]
	global_store_dword v[34:35], v36, off
	v_lshl_add_u64 v[32:33], v[32:33], 0, s[20:21]
	v_add_f32_e32 v34, v123, v38
	v_min_f32_e32 v35, 0, v34
	v_mul_f32_e64 v34, |v34|, s34
	v_exp_f32_e32 v34, v34
	s_nop 0
	v_add_f32_e32 v34, 1.0, v34
	v_log_f32_e32 v34, v34
	s_nop 0
	v_fmac_f32_e32 v35, 0xbf317218, v34
	global_store_dword v[32:33], v35, off
.LBB0_316:
	s_or_b64 exec, exec, s[6:7]
	v_mov_b32_e32 v85, v185
	v_mov_b32_e32 v48, v185
	s_waitcnt vmcnt(20)
	v_mov_b32_e32 v34, v158
	v_mov_b32_e32 v36, v159
	v_mov_b32_e32 v37, v160
	v_mov_b32_e32 v38, v161
	v_mov_b32_e32 v39, v162
	v_mov_b32_e32 v40, v163
	v_mov_b32_e32 v41, v164
	v_mov_b32_e32 v42, v165
	s_andn2_b64 vcc, exec, s[14:15]
	v_lshlrev_b32_e32 v32, 16, v34
	v_and_b32_e32 v33, 0xffff0000, v34
	v_pk_mul_f32 v[34:35], v[32:33], v[32:33]
	s_nop 0
	v_add_f32_e32 v34, v34, v35
	s_nop 1
	v_add_f32_dpp v34, v34, v34 row_shr:1 row_mask:0xf bank_mask:0xf bound_ctrl:1
	s_nop 1
	v_add_f32_dpp v34, v34, v34 row_shr:2 row_mask:0xf bank_mask:0xf bound_ctrl:1
	s_nop 1
	v_add_f32_dpp v34, v34, v34 row_shr:4 row_mask:0xf bank_mask:0xf bound_ctrl:1
	s_nop 1
	v_add_f32_dpp v34, v34, v34 row_shr:8 row_mask:0xf bank_mask:0xf bound_ctrl:1
	s_nop 0
	v_readlane_b32 s20, v34, 31
	v_readlane_b32 s21, v34, 63
	v_readlane_b32 s6, v34, 15
	v_readlane_b32 s7, v34, 47
	v_mov_b32_e32 v34, s20
	v_mov_b32_e32 v35, s21
	v_pk_add_f32 v[34:35], s[6:7], v[34:35]
	s_nop 0
	v_add_f32_e32 v34, v34, v35
	v_fmamk_f32 v34, v34, 0x3c000000, v252
	v_rsq_f32_e32 v34, v34
	s_nop 0
	v_pk_mul_f32 v[32:33], v[34:35], v[32:33] op_sel_hi:[0,1]
	v_pk_mul_f32 v[32:33], v[64:65], v[32:33]
	s_nop 0
	v_cvt_pk_bf16_f32 v43, v32, v33
	v_lshlrev_b32_e32 v32, 16, v36
	v_and_b32_e32 v33, 0xffff0000, v36
	v_pk_mul_f32 v[34:35], v[32:33], v[32:33]
	s_nop 0
	v_add_f32_e32 v34, v34, v35
	s_nop 1
	v_add_f32_dpp v34, v34, v34 row_shr:1 row_mask:0xf bank_mask:0xf bound_ctrl:1
	s_nop 1
	v_add_f32_dpp v34, v34, v34 row_shr:2 row_mask:0xf bank_mask:0xf bound_ctrl:1
	s_nop 1
	v_add_f32_dpp v34, v34, v34 row_shr:4 row_mask:0xf bank_mask:0xf bound_ctrl:1
	s_nop 1
	v_add_f32_dpp v34, v34, v34 row_shr:8 row_mask:0xf bank_mask:0xf bound_ctrl:1
	s_nop 0
	v_readlane_b32 s20, v34, 31
	v_readlane_b32 s21, v34, 63
	v_readlane_b32 s6, v34, 15
	v_readlane_b32 s7, v34, 47
	v_mov_b32_e32 v34, s20
	v_mov_b32_e32 v35, s21
	v_pk_add_f32 v[34:35], s[6:7], v[34:35]
	s_nop 0
	v_add_f32_e32 v34, v34, v35
	v_fmamk_f32 v34, v34, 0x3c000000, v252
	v_rsq_f32_e32 v34, v34
	s_nop 0
	v_pk_mul_f32 v[32:33], v[34:35], v[32:33] op_sel_hi:[0,1]
	v_pk_mul_f32 v[32:33], v[64:65], v[32:33]
	s_nop 0
	v_cvt_pk_bf16_f32 v32, v32, v33
	ds_write2_b32 v100, v43, v32 offset1:68
	v_lshlrev_b32_e32 v32, 16, v37
	v_and_b32_e32 v33, 0xffff0000, v37
	v_pk_mul_f32 v[34:35], v[32:33], v[32:33]
	v_add_u32_e32 v37, 0x400, v100
	v_add_f32_e32 v34, v34, v35
	s_nop 1
	v_add_f32_dpp v34, v34, v34 row_shr:1 row_mask:0xf bank_mask:0xf bound_ctrl:1
	s_nop 1
	v_add_f32_dpp v34, v34, v34 row_shr:2 row_mask:0xf bank_mask:0xf bound_ctrl:1
	s_nop 1
	v_add_f32_dpp v34, v34, v34 row_shr:4 row_mask:0xf bank_mask:0xf bound_ctrl:1
	s_nop 1
	v_add_f32_dpp v34, v34, v34 row_shr:8 row_mask:0xf bank_mask:0xf bound_ctrl:1
	s_nop 0
	v_readlane_b32 s20, v34, 31
	v_readlane_b32 s21, v34, 63
	v_readlane_b32 s6, v34, 15
	v_readlane_b32 s7, v34, 47
	v_mov_b32_e32 v34, s20
	v_mov_b32_e32 v35, s21
	v_pk_add_f32 v[34:35], s[6:7], v[34:35]
	s_nop 0
	v_add_f32_e32 v34, v34, v35
	v_fmamk_f32 v34, v34, 0x3c000000, v252
	v_rsq_f32_e32 v34, v34
	s_nop 0
	v_pk_mul_f32 v[32:33], v[34:35], v[32:33] op_sel_hi:[0,1]
	v_pk_mul_f32 v[32:33], v[64:65], v[32:33]
	s_nop 0
	v_cvt_pk_bf16_f32 v36, v32, v33
	v_lshlrev_b32_e32 v32, 16, v38
	v_and_b32_e32 v33, 0xffff0000, v38
	v_pk_mul_f32 v[34:35], v[32:33], v[32:33]
	s_nop 0
	v_add_f32_e32 v34, v34, v35
	s_nop 1
	v_add_f32_dpp v34, v34, v34 row_shr:1 row_mask:0xf bank_mask:0xf bound_ctrl:1
	s_nop 1
	v_add_f32_dpp v34, v34, v34 row_shr:2 row_mask:0xf bank_mask:0xf bound_ctrl:1
	s_nop 1
	v_add_f32_dpp v34, v34, v34 row_shr:4 row_mask:0xf bank_mask:0xf bound_ctrl:1
	s_nop 1
	v_add_f32_dpp v34, v34, v34 row_shr:8 row_mask:0xf bank_mask:0xf bound_ctrl:1
	s_nop 0
	v_readlane_b32 s20, v34, 31
	v_readlane_b32 s21, v34, 63
	v_readlane_b32 s6, v34, 15
	v_readlane_b32 s7, v34, 47
	v_mov_b32_e32 v34, s20
	v_mov_b32_e32 v35, s21
	v_pk_add_f32 v[34:35], s[6:7], v[34:35]
	s_nop 0
	v_add_f32_e32 v34, v34, v35
	v_fmamk_f32 v34, v34, 0x3c000000, v252
	v_rsq_f32_e32 v34, v34
	s_nop 0
	v_pk_mul_f32 v[32:33], v[34:35], v[32:33] op_sel_hi:[0,1]
	v_pk_mul_f32 v[32:33], v[64:65], v[32:33]
	s_nop 0
	v_cvt_pk_bf16_f32 v32, v32, v33
	ds_write2_b32 v100, v36, v32 offset0:136 offset1:204
	v_lshlrev_b32_e32 v32, 16, v39
	v_and_b32_e32 v33, 0xffff0000, v39
	v_pk_mul_f32 v[34:35], v[32:33], v[32:33]
	s_nop 0
	v_add_f32_e32 v34, v34, v35
	s_nop 1
	v_add_f32_dpp v34, v34, v34 row_shr:1 row_mask:0xf bank_mask:0xf bound_ctrl:1
	s_nop 1
	v_add_f32_dpp v34, v34, v34 row_shr:2 row_mask:0xf bank_mask:0xf bound_ctrl:1
	s_nop 1
	v_add_f32_dpp v34, v34, v34 row_shr:4 row_mask:0xf bank_mask:0xf bound_ctrl:1
	s_nop 1
	v_add_f32_dpp v34, v34, v34 row_shr:8 row_mask:0xf bank_mask:0xf bound_ctrl:1
	s_nop 0
	v_readlane_b32 s20, v34, 31
	v_readlane_b32 s21, v34, 63
	v_readlane_b32 s6, v34, 15
	v_readlane_b32 s7, v34, 47
	v_mov_b32_e32 v34, s20
	v_mov_b32_e32 v35, s21
	v_pk_add_f32 v[34:35], s[6:7], v[34:35]
	s_nop 0
	v_add_f32_e32 v34, v34, v35
	v_fmamk_f32 v34, v34, 0x3c000000, v252
	v_rsq_f32_e32 v34, v34
	s_nop 0
	v_pk_mul_f32 v[32:33], v[34:35], v[32:33] op_sel_hi:[0,1]
	v_pk_mul_f32 v[32:33], v[64:65], v[32:33]
	s_nop 0
	v_cvt_pk_bf16_f32 v36, v32, v33
	v_lshlrev_b32_e32 v32, 16, v40
	v_and_b32_e32 v33, 0xffff0000, v40
	v_pk_mul_f32 v[34:35], v[32:33], v[32:33]
	v_mov_b32_e32 v40, v185
	v_add_f32_e32 v34, v34, v35
	s_nop 1
	v_add_f32_dpp v34, v34, v34 row_shr:1 row_mask:0xf bank_mask:0xf bound_ctrl:1
	s_nop 1
	v_add_f32_dpp v34, v34, v34 row_shr:2 row_mask:0xf bank_mask:0xf bound_ctrl:1
	s_nop 1
	v_add_f32_dpp v34, v34, v34 row_shr:4 row_mask:0xf bank_mask:0xf bound_ctrl:1
	s_nop 1
	v_add_f32_dpp v34, v34, v34 row_shr:8 row_mask:0xf bank_mask:0xf bound_ctrl:1
	s_nop 0
	v_readlane_b32 s20, v34, 31
	v_readlane_b32 s21, v34, 63
	v_readlane_b32 s6, v34, 15
	v_readlane_b32 s7, v34, 47
	v_mov_b32_e32 v34, s20
	v_mov_b32_e32 v35, s21
	v_pk_add_f32 v[34:35], s[6:7], v[34:35]
	s_nop 0
	v_add_f32_e32 v34, v34, v35
	v_fmamk_f32 v34, v34, 0x3c000000, v252
	v_rsq_f32_e32 v34, v34
	s_nop 0
	v_pk_mul_f32 v[32:33], v[34:35], v[32:33] op_sel_hi:[0,1]
	v_pk_mul_f32 v[32:33], v[64:65], v[32:33]
	s_nop 0
	v_cvt_pk_bf16_f32 v32, v32, v33
	ds_write2_b32 v37, v36, v32 offset0:16 offset1:84
	v_lshlrev_b32_e32 v32, 16, v41
	v_and_b32_e32 v33, 0xffff0000, v41
	v_pk_mul_f32 v[34:35], v[32:33], v[32:33]
	s_nop 0
	v_add_f32_e32 v34, v34, v35
	s_nop 1
	v_add_f32_dpp v34, v34, v34 row_shr:1 row_mask:0xf bank_mask:0xf bound_ctrl:1
	s_nop 1
	v_add_f32_dpp v34, v34, v34 row_shr:2 row_mask:0xf bank_mask:0xf bound_ctrl:1
	s_nop 1
	v_add_f32_dpp v34, v34, v34 row_shr:4 row_mask:0xf bank_mask:0xf bound_ctrl:1
	s_nop 1
	v_add_f32_dpp v34, v34, v34 row_shr:8 row_mask:0xf bank_mask:0xf bound_ctrl:1
	s_nop 0
	v_readlane_b32 s20, v34, 31
	v_readlane_b32 s21, v34, 63
	v_readlane_b32 s6, v34, 15
	v_readlane_b32 s7, v34, 47
	v_mov_b32_e32 v34, s20
	v_mov_b32_e32 v35, s21
	v_pk_add_f32 v[34:35], s[6:7], v[34:35]
	s_nop 0
	v_add_f32_e32 v34, v34, v35
	v_fmamk_f32 v34, v34, 0x3c000000, v252
	v_rsq_f32_e32 v34, v34
	s_nop 0
	v_pk_mul_f32 v[32:33], v[34:35], v[32:33] op_sel_hi:[0,1]
	v_pk_mul_f32 v[32:33], v[64:65], v[32:33]
	s_nop 0
	v_cvt_pk_bf16_f32 v36, v32, v33
	v_lshlrev_b32_e32 v32, 16, v42
	v_and_b32_e32 v33, 0xffff0000, v42
	v_pk_mul_f32 v[34:35], v[32:33], v[32:33]
	s_nop 0
	v_add_f32_e32 v34, v34, v35
	s_nop 1
	v_add_f32_dpp v34, v34, v34 row_shr:1 row_mask:0xf bank_mask:0xf bound_ctrl:1
	s_nop 1
	v_add_f32_dpp v34, v34, v34 row_shr:2 row_mask:0xf bank_mask:0xf bound_ctrl:1
	s_nop 1
	v_add_f32_dpp v34, v34, v34 row_shr:4 row_mask:0xf bank_mask:0xf bound_ctrl:1
	s_nop 1
	v_add_f32_dpp v34, v34, v34 row_shr:8 row_mask:0xf bank_mask:0xf bound_ctrl:1
	s_nop 0
	v_readlane_b32 s20, v34, 31
	v_readlane_b32 s21, v34, 63
	v_readlane_b32 s6, v34, 15
	v_readlane_b32 s7, v34, 47
	v_mov_b32_e32 v34, s20
	v_mov_b32_e32 v35, s21
	v_pk_add_f32 v[34:35], s[6:7], v[34:35]
	s_mov_b64 s[20:21], -1
	v_add_f32_e32 v34, v34, v35
	v_fmamk_f32 v34, v34, 0x3c000000, v252
	v_rsq_f32_e32 v34, v34
	s_nop 0
	v_pk_mul_f32 v[32:33], v[34:35], v[32:33] op_sel_hi:[0,1]
	v_pk_mul_f32 v[32:33], v[64:65], v[32:33]
	s_nop 0
	v_cvt_pk_bf16_f32 v32, v32, v33
	ds_write2_b32 v37, v36, v32 offset0:152 offset1:220
	v_mov_b32_e32 v32, v185
	v_mov_b32_e32 v36, v185
	s_waitcnt lgkmcnt(0)
	s_barrier
	ds_read_b128 v[44:47], v101
	ds_read_b128 v[52:55], v101 offset:192
	v_mov_b32_e32 v33, v32
	v_mov_b32_e32 v34, v32
	v_mov_b32_e32 v35, v32
	v_mov_b32_e32 v41, v40
	v_mov_b32_e32 v42, v40
	v_mov_b32_e32 v43, v40
	s_waitcnt lgkmcnt(1)
	v_mfma_f32_16x16x32_bf16 v[32:35], v[28:31], v[44:47], v[32:35]
	v_mov_b32_e32 v37, v36
	v_mov_b32_e32 v38, v36
	v_mov_b32_e32 v39, v36
	v_mfma_f32_16x16x32_bf16 v[40:43], v[12:15], v[44:47], v[40:43]
	ds_read_b128 v[44:47], v101 offset:64
	v_mov_b32_e32 v49, v48
	v_mov_b32_e32 v50, v48
	s_waitcnt lgkmcnt(0)
	v_mfma_f32_16x16x32_bf16 v[32:35], v[24:27], v[44:47], v[32:35]
	v_mov_b32_e32 v51, v48
	v_mfma_f32_16x16x32_bf16 v[40:43], v[8:11], v[44:47], v[40:43]
	ds_read_b128 v[44:47], v101 offset:128
	s_waitcnt lgkmcnt(0)
	v_mfma_f32_16x16x32_bf16 v[32:35], v[20:23], v[44:47], v[32:35]
	v_mfma_f32_16x16x32_bf16 v[40:43], v[4:7], v[44:47], v[40:43]
	v_mfma_f32_16x16x32_bf16 v[44:47], v[16:19], v[52:55], v[32:35]
	s_nop 5
	ds_read_b128 v[32:35], v101 offset:4352
	s_waitcnt lgkmcnt(0)
	v_mfma_f32_16x16x32_bf16 v[36:39], v[28:31], v[32:35], v[36:39]
	v_mfma_f32_16x16x32_bf16 v[32:35], v[12:15], v[32:35], v[48:51]
	s_nop 2
	ds_read_b128 v[48:51], v101 offset:4416
	s_waitcnt lgkmcnt(0)
	v_mfma_f32_16x16x32_bf16 v[36:39], v[24:27], v[48:51], v[36:39]
	v_mfma_f32_16x16x32_bf16 v[32:35], v[8:11], v[48:51], v[32:35]
	ds_read_b128 v[48:51], v101 offset:4480
	s_waitcnt lgkmcnt(0)
	v_mfma_f32_16x16x32_bf16 v[36:39], v[20:23], v[48:51], v[36:39]
	v_mfma_f32_16x16x32_bf16 v[32:35], v[4:7], v[48:51], v[32:35]
	ds_read_b128 v[48:51], v101 offset:4544
	v_mfma_f32_16x16x32_bf16 v[40:43], v[0:3], v[52:55], v[40:43]
	s_waitcnt lgkmcnt(0)
	v_mfma_f32_16x16x32_bf16 v[36:39], v[16:19], v[48:51], v[36:39]
	v_mfma_f32_16x16x32_bf16 v[32:35], v[0:3], v[48:51], v[32:35]
	v_cndmask_b32_e64 v48, 0, 1, s[14:15]
	v_cmp_ne_u32_e64 s[6:7], 1, v48
	s_cbranch_vccnz .LBB0_320
	v_bfe_u32 v48, v44, 16, 1
	s_movk_i32 s20, 0x7fff
	v_add3_u32 v48, v44, v48, s20
	ds_write_b16_d16_hi v102, v48 offset:32768
	v_bfe_u32 v48, v45, 16, 1
	v_add3_u32 v48, v45, v48, s20
	ds_write_b16_d16_hi v102, v48 offset:32912
	v_bfe_u32 v48, v46, 16, 1
	v_add3_u32 v48, v46, v48, s20
	ds_write_b16_d16_hi v102, v48 offset:33056
	v_bfe_u32 v48, v47, 16, 1
	v_add3_u32 v48, v47, v48, s20
	ds_write_b16_d16_hi v102, v48 offset:33200
	v_bfe_u32 v48, v40, 16, 1
	v_add3_u32 v48, v40, v48, s20
	ds_write_b16_d16_hi v102, v48 offset:37376
	v_bfe_u32 v48, v41, 16, 1
	v_add3_u32 v48, v41, v48, s20
	ds_write_b16_d16_hi v102, v48 offset:37520
	v_bfe_u32 v48, v42, 16, 1
	v_add3_u32 v48, v42, v48, s20
	ds_write_b16_d16_hi v102, v48 offset:37664
	v_bfe_u32 v48, v43, 16, 1
	v_add3_u32 v48, v43, v48, s20
	ds_write_b16_d16_hi v102, v48 offset:37808
	s_cbranch_execz .LBB0_321

.LBB0_321:
	s_waitcnt vmcnt(16)
	v_mov_b64_e32 v[48:49], v[166:167]
	v_mov_b64_e32 v[50:51], v[168:169]
	v_mov_b64_e32 v[52:53], v[170:171]
	v_mov_b64_e32 v[54:55], v[172:173]
	s_nop 4
	v_pk_mul_f32 v[56:57], v[42:43], v[54:55]
	v_pk_mul_f32 v[58:59], v[40:41], v[52:53]
	v_pk_fma_f32 v[56:57], v[46:47], v[50:51], v[56:57] neg_lo:[0,0,1] neg_hi:[0,0,1]
	v_pk_fma_f32 v[58:59], v[44:45], v[48:49], v[58:59] neg_lo:[0,0,1] neg_hi:[0,0,1]
	v_pk_mul_f32 v[46:47], v[46:47], v[54:55]
	v_pk_mul_f32 v[44:45], v[44:45], v[52:53]
	v_pk_fma_f32 v[42:43], v[42:43], v[50:51], v[46:47]
	v_pk_fma_f32 v[40:41], v[40:41], v[48:49], v[44:45]
	v_cvt_pk_bf16_f32 v44, v58, v59
	v_cvt_pk_bf16_f32 v40, v40, v41
	v_cvt_pk_bf16_f32 v41, v42, v43
	v_add_u32_e32 v42, s25, v97
	v_ashrrev_i32_e32 v43, 31, v42
	v_lshlrev_b64 v[42:43], 7, v[42:43]
	v_cvt_pk_bf16_f32 v45, v56, v57
	v_lshl_add_u64 v[42:43], v[78:79], 0, v[42:43]
	global_store_dwordx2 v[42:43], v[44:45], off
	global_store_dwordx2 v[42:43], v[40:41], off offset:64
	s_and_b64 vcc, exec, s[6:7]
	s_mov_b64 s[6:7], -1
	s_cbranch_vccz .LBB0_319

.LBB0_323:
	s_waitcnt vmcnt(16)
	v_mov_b64_e32 v[40:41], v[174:175]
	v_mov_b64_e32 v[42:43], v[176:177]
	v_mov_b64_e32 v[44:45], v[178:179]
	v_mov_b64_e32 v[46:47], v[180:181]
	s_nop 4
	v_pk_mul_f32 v[48:49], v[34:35], v[46:47]
	v_pk_mul_f32 v[50:51], v[32:33], v[44:45]
	v_pk_fma_f32 v[48:49], v[38:39], v[42:43], v[48:49] neg_lo:[0,0,1] neg_hi:[0,0,1]
	v_pk_fma_f32 v[50:51], v[36:37], v[40:41], v[50:51] neg_lo:[0,0,1] neg_hi:[0,0,1]
	v_pk_mul_f32 v[38:39], v[38:39], v[46:47]
	v_pk_mul_f32 v[36:37], v[36:37], v[44:45]
	v_pk_fma_f32 v[34:35], v[34:35], v[42:43], v[38:39]
	v_pk_fma_f32 v[32:33], v[32:33], v[40:41], v[36:37]
	v_cvt_pk_bf16_f32 v36, v50, v51
	v_cvt_pk_bf16_f32 v32, v32, v33
	v_cvt_pk_bf16_f32 v33, v34, v35
	v_add3_u32 v34, v97, s25, 16
	v_ashrrev_i32_e32 v35, 31, v34
	v_lshlrev_b64 v[34:35], 7, v[34:35]
	v_cvt_pk_bf16_f32 v37, v48, v49
	v_lshl_add_u64 v[34:35], v[78:79], 0, v[34:35]
	global_store_dwordx2 v[34:35], v[36:37], off
	global_store_dwordx2 v[34:35], v[32:33], off offset:64
	s_branch .LBB0_309
